# attention unit epilogues (global, NA, window): output rows written as 32 paired dword stores per lane (DPP neighbour exchange + v_cvt_pk_bf16_f32) instead of 64 two-byte stores
# baseline (speedup 1.0000x reference)
.LBB0_582:
	s_or_b64 exec, exec, s[2:3]
	s_waitcnt lgkmcnt(0)
	v_add_u32_e32 v72, v144, v184
	ds_read_b128 v[64:67], v72
	ds_read_b128 v[68:71], v72 offset:32
	s_add_u32 s0, s20, s0
	v_ashrrev_i32_e32 v183, 31, v182
	s_addc_u32 s1, s21, s1
	s_waitcnt lgkmcnt(1)
	v_rcp_f32_e32 v73, v64
	v_rcp_f32_e32 v74, v65
	v_rcp_f32_e32 v75, v66
	v_rcp_f32_e32 v76, v67
	ds_read_b128 v[64:67], v72 offset:64
	s_waitcnt lgkmcnt(1)
	v_rcp_f32_e32 v77, v68
	v_rcp_f32_e32 v78, v69
	v_rcp_f32_e32 v79, v70
	v_rcp_f32_e32 v80, v71
	ds_read_b128 v[68:71], v72 offset:96
	s_waitcnt lgkmcnt(1)
	v_rcp_f32_e32 v72, v64
	v_rcp_f32_e32 v81, v65
	v_lshlrev_b64 v[64:65], 12, v[182:183]
	v_lshl_add_u64 v[64:65], s[0:1], 0, v[64:65]
	v_lshlrev_b32_e32 v192, 1, v200
	v_rcp_f32_e32 v82, v66
	v_rcp_f32_e32 v83, v67
	v_lshlrev_b32_e32 v66, 14, v201
	v_lshl_add_u64 v[64:65], v[64:65], 0, v[192:193]
	v_mov_b32_e32 v67, v193
	v_lshl_add_u64 v[64:65], v[64:65], 0, v[66:67]
	s_movk_i32 s1, 0x7fff
	v_add_u32_e32 v116, v144, v184
	ds_read_b128 v[100:103], v116
	ds_read_b128 v[104:107], v116 offset:32
	ds_read_b128 v[108:111], v116 offset:64
	ds_read_b128 v[112:115], v116 offset:96
	v_and_b32_e32 v117, 1, v200
	v_cmp_eq_u32_e64 s[100:101], 1, v117
	v_mov_b32_e32 v118, 0xffe
	v_cndmask_b32_e64 v118, 0, v118, s[100:101]
	v_mov_b32_e32 v119, 0
	v_lshl_add_u64 v[120:121], v[64:65], 0, v[118:119]
	v_mov_b32_e32 v125, 0
	s_waitcnt lgkmcnt(0)
	v_rcp_f32_e32 v100, v100
	v_rcp_f32_e32 v101, v101
	v_rcp_f32_e32 v102, v102
	v_rcp_f32_e32 v103, v103
	v_rcp_f32_e32 v104, v104
	v_rcp_f32_e32 v105, v105
	v_rcp_f32_e32 v106, v106
	v_rcp_f32_e32 v107, v107
	v_rcp_f32_e32 v108, v108
	v_rcp_f32_e32 v109, v109
	v_rcp_f32_e32 v110, v110
	v_rcp_f32_e32 v111, v111
	v_rcp_f32_e32 v112, v112
	v_rcp_f32_e32 v113, v113
	v_rcp_f32_e32 v114, v114
	v_rcp_f32_e32 v115, v115
	v_mul_f32_e32 v126, v0, v100
	v_mul_f32_e32 v127, v1, v101
	s_nop 1
	v_mov_b32_dpp v128, v126 quad_perm:[1,0,3,2] row_mask:0xf bank_mask:0xf
	v_mov_b32_dpp v129, v127 quad_perm:[1,0,3,2] row_mask:0xf bank_mask:0xf
	v_cndmask_b32_e64 v130, v126, v129, s[100:101]
	v_cndmask_b32_e64 v131, v128, v127, s[100:101]
	v_cvt_pk_bf16_f32 v130, v130, v131
	global_store_dword v[120:121], v130, off offset:1536
	v_mul_f32_e32 v126, v16, v100
	v_mul_f32_e32 v127, v17, v101
	s_nop 1
	v_mov_b32_dpp v128, v126 quad_perm:[1,0,3,2] row_mask:0xf bank_mask:0xf
	v_mov_b32_dpp v129, v127 quad_perm:[1,0,3,2] row_mask:0xf bank_mask:0xf
	v_cndmask_b32_e64 v130, v126, v129, s[100:101]
	v_cndmask_b32_e64 v131, v128, v127, s[100:101]
	v_cvt_pk_bf16_f32 v130, v130, v131
	global_store_dword v[120:121], v130, off offset:1600
	v_mul_f32_e32 v126, v32, v100
	v_mul_f32_e32 v127, v33, v101
	s_nop 1
	v_mov_b32_dpp v128, v126 quad_perm:[1,0,3,2] row_mask:0xf bank_mask:0xf
	v_mov_b32_dpp v129, v127 quad_perm:[1,0,3,2] row_mask:0xf bank_mask:0xf
	v_cndmask_b32_e64 v130, v126, v129, s[100:101]
	v_cndmask_b32_e64 v131, v128, v127, s[100:101]
	v_cvt_pk_bf16_f32 v130, v130, v131
	global_store_dword v[120:121], v130, off offset:1664
	v_mul_f32_e32 v126, v48, v100
	v_mul_f32_e32 v127, v49, v101
	s_nop 1
	v_mov_b32_dpp v128, v126 quad_perm:[1,0,3,2] row_mask:0xf bank_mask:0xf
	v_mov_b32_dpp v129, v127 quad_perm:[1,0,3,2] row_mask:0xf bank_mask:0xf
	v_cndmask_b32_e64 v130, v126, v129, s[100:101]
	v_cndmask_b32_e64 v131, v128, v127, s[100:101]
	v_cvt_pk_bf16_f32 v130, v130, v131
	global_store_dword v[120:121], v130, off offset:1728
	v_mov_b32_e32 v124, 0x2000
	v_lshl_add_u64 v[122:123], v[120:121], 0, v[124:125]
	v_mul_f32_e32 v126, v2, v102
	v_mul_f32_e32 v127, v3, v103
	s_nop 1
	v_mov_b32_dpp v128, v126 quad_perm:[1,0,3,2] row_mask:0xf bank_mask:0xf
	v_mov_b32_dpp v129, v127 quad_perm:[1,0,3,2] row_mask:0xf bank_mask:0xf
	v_cndmask_b32_e64 v130, v126, v129, s[100:101]
	v_cndmask_b32_e64 v131, v128, v127, s[100:101]
	v_cvt_pk_bf16_f32 v130, v130, v131
	global_store_dword v[122:123], v130, off offset:1536
	v_mul_f32_e32 v126, v18, v102
	v_mul_f32_e32 v127, v19, v103
	s_nop 1
	v_mov_b32_dpp v128, v126 quad_perm:[1,0,3,2] row_mask:0xf bank_mask:0xf
	v_mov_b32_dpp v129, v127 quad_perm:[1,0,3,2] row_mask:0xf bank_mask:0xf
	v_cndmask_b32_e64 v130, v126, v129, s[100:101]
	v_cndmask_b32_e64 v131, v128, v127, s[100:101]
	v_cvt_pk_bf16_f32 v130, v130, v131
	global_store_dword v[122:123], v130, off offset:1600
	v_mul_f32_e32 v126, v34, v102
	v_mul_f32_e32 v127, v35, v103
	s_nop 1
	v_mov_b32_dpp v128, v126 quad_perm:[1,0,3,2] row_mask:0xf bank_mask:0xf
	v_mov_b32_dpp v129, v127 quad_perm:[1,0,3,2] row_mask:0xf bank_mask:0xf
	v_cndmask_b32_e64 v130, v126, v129, s[100:101]
	v_cndmask_b32_e64 v131, v128, v127, s[100:101]
	v_cvt_pk_bf16_f32 v130, v130, v131
	global_store_dword v[122:123], v130, off offset:1664
	v_mul_f32_e32 v126, v50, v102
	v_mul_f32_e32 v127, v51, v103
	s_nop 1
	v_mov_b32_dpp v128, v126 quad_perm:[1,0,3,2] row_mask:0xf bank_mask:0xf
	v_mov_b32_dpp v129, v127 quad_perm:[1,0,3,2] row_mask:0xf bank_mask:0xf
	v_cndmask_b32_e64 v130, v126, v129, s[100:101]
	v_cndmask_b32_e64 v131, v128, v127, s[100:101]
	v_cvt_pk_bf16_f32 v130, v130, v131
	global_store_dword v[122:123], v130, off offset:1728
	v_mov_b32_e32 v124, 0x8000
	v_lshl_add_u64 v[122:123], v[120:121], 0, v[124:125]
	v_mul_f32_e32 v126, v4, v104
	v_mul_f32_e32 v127, v5, v105
	s_nop 1
	v_mov_b32_dpp v128, v126 quad_perm:[1,0,3,2] row_mask:0xf bank_mask:0xf
	v_mov_b32_dpp v129, v127 quad_perm:[1,0,3,2] row_mask:0xf bank_mask:0xf
	v_cndmask_b32_e64 v130, v126, v129, s[100:101]
	v_cndmask_b32_e64 v131, v128, v127, s[100:101]
	v_cvt_pk_bf16_f32 v130, v130, v131
	global_store_dword v[122:123], v130, off offset:1536
	v_mul_f32_e32 v126, v20, v104
	v_mul_f32_e32 v127, v21, v105
	s_nop 1
	v_mov_b32_dpp v128, v126 quad_perm:[1,0,3,2] row_mask:0xf bank_mask:0xf
	v_mov_b32_dpp v129, v127 quad_perm:[1,0,3,2] row_mask:0xf bank_mask:0xf
	v_cndmask_b32_e64 v130, v126, v129, s[100:101]
	v_cndmask_b32_e64 v131, v128, v127, s[100:101]
	v_cvt_pk_bf16_f32 v130, v130, v131
	global_store_dword v[122:123], v130, off offset:1600
	v_mul_f32_e32 v126, v36, v104
	v_mul_f32_e32 v127, v37, v105
	s_nop 1
	v_mov_b32_dpp v128, v126 quad_perm:[1,0,3,2] row_mask:0xf bank_mask:0xf
	v_mov_b32_dpp v129, v127 quad_perm:[1,0,3,2] row_mask:0xf bank_mask:0xf
	v_cndmask_b32_e64 v130, v126, v129, s[100:101]
	v_cndmask_b32_e64 v131, v128, v127, s[100:101]
	v_cvt_pk_bf16_f32 v130, v130, v131
	global_store_dword v[122:123], v130, off offset:1664
	v_mul_f32_e32 v126, v52, v104
	v_mul_f32_e32 v127, v53, v105
	s_nop 1
	v_mov_b32_dpp v128, v126 quad_perm:[1,0,3,2] row_mask:0xf bank_mask:0xf
	v_mov_b32_dpp v129, v127 quad_perm:[1,0,3,2] row_mask:0xf bank_mask:0xf
	v_cndmask_b32_e64 v130, v126, v129, s[100:101]
	v_cndmask_b32_e64 v131, v128, v127, s[100:101]
	v_cvt_pk_bf16_f32 v130, v130, v131
	global_store_dword v[122:123], v130, off offset:1728
	v_mov_b32_e32 v124, 0xa000
	v_lshl_add_u64 v[122:123], v[120:121], 0, v[124:125]
	v_mul_f32_e32 v126, v6, v106
	v_mul_f32_e32 v127, v7, v107
	s_nop 1
	v_mov_b32_dpp v128, v126 quad_perm:[1,0,3,2] row_mask:0xf bank_mask:0xf
	v_mov_b32_dpp v129, v127 quad_perm:[1,0,3,2] row_mask:0xf bank_mask:0xf
	v_cndmask_b32_e64 v130, v126, v129, s[100:101]
	v_cndmask_b32_e64 v131, v128, v127, s[100:101]
	v_cvt_pk_bf16_f32 v130, v130, v131
	global_store_dword v[122:123], v130, off offset:1536
	v_mul_f32_e32 v126, v22, v106
	v_mul_f32_e32 v127, v23, v107
	s_nop 1
	v_mov_b32_dpp v128, v126 quad_perm:[1,0,3,2] row_mask:0xf bank_mask:0xf
	v_mov_b32_dpp v129, v127 quad_perm:[1,0,3,2] row_mask:0xf bank_mask:0xf
	v_cndmask_b32_e64 v130, v126, v129, s[100:101]
	v_cndmask_b32_e64 v131, v128, v127, s[100:101]
	v_cvt_pk_bf16_f32 v130, v130, v131
	global_store_dword v[122:123], v130, off offset:1600
	v_mul_f32_e32 v126, v38, v106
	v_mul_f32_e32 v127, v39, v107
	s_nop 1
	v_mov_b32_dpp v128, v126 quad_perm:[1,0,3,2] row_mask:0xf bank_mask:0xf
	v_mov_b32_dpp v129, v127 quad_perm:[1,0,3,2] row_mask:0xf bank_mask:0xf
	v_cndmask_b32_e64 v130, v126, v129, s[100:101]
	v_cndmask_b32_e64 v131, v128, v127, s[100:101]
	v_cvt_pk_bf16_f32 v130, v130, v131
	global_store_dword v[122:123], v130, off offset:1664
	v_mul_f32_e32 v126, v54, v106
	v_mul_f32_e32 v127, v55, v107
	s_nop 1
	v_mov_b32_dpp v128, v126 quad_perm:[1,0,3,2] row_mask:0xf bank_mask:0xf
	v_mov_b32_dpp v129, v127 quad_perm:[1,0,3,2] row_mask:0xf bank_mask:0xf
	v_cndmask_b32_e64 v130, v126, v129, s[100:101]
	v_cndmask_b32_e64 v131, v128, v127, s[100:101]
	v_cvt_pk_bf16_f32 v130, v130, v131
	global_store_dword v[122:123], v130, off offset:1728
	v_mov_b32_e32 v124, 0x10000
	v_lshl_add_u64 v[122:123], v[120:121], 0, v[124:125]
	v_mul_f32_e32 v126, v8, v108
	v_mul_f32_e32 v127, v9, v109
	s_nop 1
	v_mov_b32_dpp v128, v126 quad_perm:[1,0,3,2] row_mask:0xf bank_mask:0xf
	v_mov_b32_dpp v129, v127 quad_perm:[1,0,3,2] row_mask:0xf bank_mask:0xf
	v_cndmask_b32_e64 v130, v126, v129, s[100:101]
	v_cndmask_b32_e64 v131, v128, v127, s[100:101]
	v_cvt_pk_bf16_f32 v130, v130, v131
	global_store_dword v[122:123], v130, off offset:1536
	v_mul_f32_e32 v126, v24, v108
	v_mul_f32_e32 v127, v25, v109
	s_nop 1
	v_mov_b32_dpp v128, v126 quad_perm:[1,0,3,2] row_mask:0xf bank_mask:0xf
	v_mov_b32_dpp v129, v127 quad_perm:[1,0,3,2] row_mask:0xf bank_mask:0xf
	v_cndmask_b32_e64 v130, v126, v129, s[100:101]
	v_cndmask_b32_e64 v131, v128, v127, s[100:101]
	v_cvt_pk_bf16_f32 v130, v130, v131
	global_store_dword v[122:123], v130, off offset:1600
	v_mul_f32_e32 v126, v40, v108
	v_mul_f32_e32 v127, v41, v109
	s_nop 1
	v_mov_b32_dpp v128, v126 quad_perm:[1,0,3,2] row_mask:0xf bank_mask:0xf
	v_mov_b32_dpp v129, v127 quad_perm:[1,0,3,2] row_mask:0xf bank_mask:0xf
	v_cndmask_b32_e64 v130, v126, v129, s[100:101]
	v_cndmask_b32_e64 v131, v128, v127, s[100:101]
	v_cvt_pk_bf16_f32 v130, v130, v131
	global_store_dword v[122:123], v130, off offset:1664
	v_mul_f32_e32 v126, v56, v108
	v_mul_f32_e32 v127, v57, v109
	s_nop 1
	v_mov_b32_dpp v128, v126 quad_perm:[1,0,3,2] row_mask:0xf bank_mask:0xf
	v_mov_b32_dpp v129, v127 quad_perm:[1,0,3,2] row_mask:0xf bank_mask:0xf
	v_cndmask_b32_e64 v130, v126, v129, s[100:101]
	v_cndmask_b32_e64 v131, v128, v127, s[100:101]
	v_cvt_pk_bf16_f32 v130, v130, v131
	global_store_dword v[122:123], v130, off offset:1728
	v_mov_b32_e32 v124, 0x12000
	v_lshl_add_u64 v[122:123], v[120:121], 0, v[124:125]
	v_mul_f32_e32 v126, v10, v110
	v_mul_f32_e32 v127, v11, v111
	s_nop 1
	v_mov_b32_dpp v128, v126 quad_perm:[1,0,3,2] row_mask:0xf bank_mask:0xf
	v_mov_b32_dpp v129, v127 quad_perm:[1,0,3,2] row_mask:0xf bank_mask:0xf
	v_cndmask_b32_e64 v130, v126, v129, s[100:101]
	v_cndmask_b32_e64 v131, v128, v127, s[100:101]
	v_cvt_pk_bf16_f32 v130, v130, v131
	global_store_dword v[122:123], v130, off offset:1536
	v_mul_f32_e32 v126, v26, v110
	v_mul_f32_e32 v127, v27, v111
	s_nop 1
	v_mov_b32_dpp v128, v126 quad_perm:[1,0,3,2] row_mask:0xf bank_mask:0xf
	v_mov_b32_dpp v129, v127 quad_perm:[1,0,3,2] row_mask:0xf bank_mask:0xf
	v_cndmask_b32_e64 v130, v126, v129, s[100:101]
	v_cndmask_b32_e64 v131, v128, v127, s[100:101]
	v_cvt_pk_bf16_f32 v130, v130, v131
	global_store_dword v[122:123], v130, off offset:1600
	v_mul_f32_e32 v126, v42, v110
	v_mul_f32_e32 v127, v43, v111
	s_nop 1
	v_mov_b32_dpp v128, v126 quad_perm:[1,0,3,2] row_mask:0xf bank_mask:0xf
	v_mov_b32_dpp v129, v127 quad_perm:[1,0,3,2] row_mask:0xf bank_mask:0xf
	v_cndmask_b32_e64 v130, v126, v129, s[100:101]
	v_cndmask_b32_e64 v131, v128, v127, s[100:101]
	v_cvt_pk_bf16_f32 v130, v130, v131
	global_store_dword v[122:123], v130, off offset:1664
	v_mul_f32_e32 v126, v58, v110
	v_mul_f32_e32 v127, v59, v111
	s_nop 1
	v_mov_b32_dpp v128, v126 quad_perm:[1,0,3,2] row_mask:0xf bank_mask:0xf
	v_mov_b32_dpp v129, v127 quad_perm:[1,0,3,2] row_mask:0xf bank_mask:0xf
	v_cndmask_b32_e64 v130, v126, v129, s[100:101]
	v_cndmask_b32_e64 v131, v128, v127, s[100:101]
	v_cvt_pk_bf16_f32 v130, v130, v131
	global_store_dword v[122:123], v130, off offset:1728
	v_mov_b32_e32 v124, 0x18000
	v_lshl_add_u64 v[122:123], v[120:121], 0, v[124:125]
	v_mul_f32_e32 v126, v12, v112
	v_mul_f32_e32 v127, v13, v113
	s_nop 1
	v_mov_b32_dpp v128, v126 quad_perm:[1,0,3,2] row_mask:0xf bank_mask:0xf
	v_mov_b32_dpp v129, v127 quad_perm:[1,0,3,2] row_mask:0xf bank_mask:0xf
	v_cndmask_b32_e64 v130, v126, v129, s[100:101]
	v_cndmask_b32_e64 v131, v128, v127, s[100:101]
	v_cvt_pk_bf16_f32 v130, v130, v131
	global_store_dword v[122:123], v130, off offset:1536
	v_mul_f32_e32 v126, v28, v112
	v_mul_f32_e32 v127, v29, v113
	s_nop 1
	v_mov_b32_dpp v128, v126 quad_perm:[1,0,3,2] row_mask:0xf bank_mask:0xf
	v_mov_b32_dpp v129, v127 quad_perm:[1,0,3,2] row_mask:0xf bank_mask:0xf
	v_cndmask_b32_e64 v130, v126, v129, s[100:101]
	v_cndmask_b32_e64 v131, v128, v127, s[100:101]
	v_cvt_pk_bf16_f32 v130, v130, v131
	global_store_dword v[122:123], v130, off offset:1600
	v_mul_f32_e32 v126, v44, v112
	v_mul_f32_e32 v127, v45, v113
	s_nop 1
	v_mov_b32_dpp v128, v126 quad_perm:[1,0,3,2] row_mask:0xf bank_mask:0xf
	v_mov_b32_dpp v129, v127 quad_perm:[1,0,3,2] row_mask:0xf bank_mask:0xf
	v_cndmask_b32_e64 v130, v126, v129, s[100:101]
	v_cndmask_b32_e64 v131, v128, v127, s[100:101]
	v_cvt_pk_bf16_f32 v130, v130, v131
	global_store_dword v[122:123], v130, off offset:1664
	v_mul_f32_e32 v126, v60, v112
	v_mul_f32_e32 v127, v61, v113
	s_nop 1
	v_mov_b32_dpp v128, v126 quad_perm:[1,0,3,2] row_mask:0xf bank_mask:0xf
	v_mov_b32_dpp v129, v127 quad_perm:[1,0,3,2] row_mask:0xf bank_mask:0xf
	v_cndmask_b32_e64 v130, v126, v129, s[100:101]
	v_cndmask_b32_e64 v131, v128, v127, s[100:101]
	v_cvt_pk_bf16_f32 v130, v130, v131
	global_store_dword v[122:123], v130, off offset:1728
	v_mov_b32_e32 v124, 0x1a000
	v_lshl_add_u64 v[122:123], v[120:121], 0, v[124:125]
	v_mul_f32_e32 v126, v14, v114
	v_mul_f32_e32 v127, v15, v115
	s_nop 1
	v_mov_b32_dpp v128, v126 quad_perm:[1,0,3,2] row_mask:0xf bank_mask:0xf
	v_mov_b32_dpp v129, v127 quad_perm:[1,0,3,2] row_mask:0xf bank_mask:0xf
	v_cndmask_b32_e64 v130, v126, v129, s[100:101]
	v_cndmask_b32_e64 v131, v128, v127, s[100:101]
	v_cvt_pk_bf16_f32 v130, v130, v131
	global_store_dword v[122:123], v130, off offset:1536
	v_mul_f32_e32 v126, v30, v114
	v_mul_f32_e32 v127, v31, v115
	s_nop 1
	v_mov_b32_dpp v128, v126 quad_perm:[1,0,3,2] row_mask:0xf bank_mask:0xf
	v_mov_b32_dpp v129, v127 quad_perm:[1,0,3,2] row_mask:0xf bank_mask:0xf
	v_cndmask_b32_e64 v130, v126, v129, s[100:101]
	v_cndmask_b32_e64 v131, v128, v127, s[100:101]
	v_cvt_pk_bf16_f32 v130, v130, v131
	global_store_dword v[122:123], v130, off offset:1600
	v_mul_f32_e32 v126, v46, v114
	v_mul_f32_e32 v127, v47, v115
	s_nop 1
	v_mov_b32_dpp v128, v126 quad_perm:[1,0,3,2] row_mask:0xf bank_mask:0xf
	v_mov_b32_dpp v129, v127 quad_perm:[1,0,3,2] row_mask:0xf bank_mask:0xf
	v_cndmask_b32_e64 v130, v126, v129, s[100:101]
	v_cndmask_b32_e64 v131, v128, v127, s[100:101]
	v_cvt_pk_bf16_f32 v130, v130, v131
	global_store_dword v[122:123], v130, off offset:1664
	v_mul_f32_e32 v126, v62, v114
	v_mul_f32_e32 v127, v63, v115
	s_nop 1
	v_mov_b32_dpp v128, v126 quad_perm:[1,0,3,2] row_mask:0xf bank_mask:0xf
	v_mov_b32_dpp v129, v127 quad_perm:[1,0,3,2] row_mask:0xf bank_mask:0xf
	v_cndmask_b32_e64 v130, v126, v129, s[100:101]
	v_cndmask_b32_e64 v131, v128, v127, s[100:101]
	v_cvt_pk_bf16_f32 v130, v130, v131
	global_store_dword v[122:123], v130, off offset:1728
	s_waitcnt vmcnt(63) expcnt(7) lgkmcnt(15)
	s_barrier

.LBB0_600:
	s_or_b64 exec, exec, s[0:1]
	s_waitcnt lgkmcnt(0)
	v_add_u32_e32 v72, v159, v148
	ds_read_b128 v[64:67], v72
	ds_read_b128 v[68:71], v72 offset:32
	v_readlane_b32 s0, v255, 10
	v_readlane_b32 s1, v255, 11
	s_lshl_b64 s[0:1], s[0:1], 12
	s_waitcnt lgkmcnt(1)
	v_rcp_f32_e32 v73, v64
	v_rcp_f32_e32 v74, v65
	v_rcp_f32_e32 v75, v66
	v_rcp_f32_e32 v76, v67
	ds_read_b128 v[64:67], v72 offset:64
	v_readlane_b32 s2, v254, 42
	s_add_u32 s0, s2, s0
	v_readlane_b32 s2, v254, 44
	s_addc_u32 s1, s2, s1
	v_readlane_b32 s2, v255, 12
	v_readlane_b32 s3, v255, 13
	s_add_u32 s0, s0, s2
	v_ashrrev_i32_e32 v153, 31, v152
	s_addc_u32 s1, s1, s3
	s_waitcnt lgkmcnt(1)
	v_rcp_f32_e32 v77, v68
	v_rcp_f32_e32 v78, v69
	v_rcp_f32_e32 v79, v70
	v_rcp_f32_e32 v80, v71
	ds_read_b128 v[68:71], v72 offset:96
	s_waitcnt lgkmcnt(1)
	v_rcp_f32_e32 v72, v64
	v_rcp_f32_e32 v81, v65
	v_lshlrev_b64 v[64:65], 12, v[152:153]
	v_lshl_add_u64 v[64:65], s[0:1], 0, v[64:65]
	v_lshlrev_b32_e32 v192, 1, v149
	v_rcp_f32_e32 v82, v66
	v_rcp_f32_e32 v83, v67
	v_lshlrev_b32_e32 v66, 14, v154
	v_lshl_add_u64 v[64:65], v[64:65], 0, v[192:193]
	v_mov_b32_e32 v67, v193
	v_lshl_add_u64 v[64:65], v[64:65], 0, v[66:67]
	s_movk_i32 s1, 0x7fff
	v_add_u32_e32 v116, v159, v148
	ds_read_b128 v[100:103], v116
	ds_read_b128 v[104:107], v116 offset:32
	ds_read_b128 v[108:111], v116 offset:64
	ds_read_b128 v[112:115], v116 offset:96
	v_and_b32_e32 v117, 1, v149
	v_cmp_eq_u32_e64 s[100:101], 1, v117
	v_mov_b32_e32 v118, 0xffe
	v_cndmask_b32_e64 v118, 0, v118, s[100:101]
	v_mov_b32_e32 v119, 0
	v_lshl_add_u64 v[120:121], v[64:65], 0, v[118:119]
	v_mov_b32_e32 v125, 0
	s_waitcnt lgkmcnt(0)
	v_rcp_f32_e32 v100, v100
	v_rcp_f32_e32 v101, v101
	v_rcp_f32_e32 v102, v102
	v_rcp_f32_e32 v103, v103
	v_rcp_f32_e32 v104, v104
	v_rcp_f32_e32 v105, v105
	v_rcp_f32_e32 v106, v106
	v_rcp_f32_e32 v107, v107
	v_rcp_f32_e32 v108, v108
	v_rcp_f32_e32 v109, v109
	v_rcp_f32_e32 v110, v110
	v_rcp_f32_e32 v111, v111
	v_rcp_f32_e32 v112, v112
	v_rcp_f32_e32 v113, v113
	v_rcp_f32_e32 v114, v114
	v_rcp_f32_e32 v115, v115
	v_mul_f32_e32 v126, v0, v100
	v_mul_f32_e32 v127, v1, v101
	s_nop 1
	v_mov_b32_dpp v128, v126 quad_perm:[1,0,3,2] row_mask:0xf bank_mask:0xf
	v_mov_b32_dpp v129, v127 quad_perm:[1,0,3,2] row_mask:0xf bank_mask:0xf
	v_cndmask_b32_e64 v130, v126, v129, s[100:101]
	v_cndmask_b32_e64 v131, v128, v127, s[100:101]
	v_cvt_pk_bf16_f32 v130, v130, v131
	global_store_dword v[120:121], v130, off
	v_mul_f32_e32 v126, v48, v100
	v_mul_f32_e32 v127, v49, v101
	s_nop 1
	v_mov_b32_dpp v128, v126 quad_perm:[1,0,3,2] row_mask:0xf bank_mask:0xf
	v_mov_b32_dpp v129, v127 quad_perm:[1,0,3,2] row_mask:0xf bank_mask:0xf
	v_cndmask_b32_e64 v130, v126, v129, s[100:101]
	v_cndmask_b32_e64 v131, v128, v127, s[100:101]
	v_cvt_pk_bf16_f32 v130, v130, v131
	global_store_dword v[120:121], v130, off offset:64
	v_mul_f32_e32 v126, v32, v100
	v_mul_f32_e32 v127, v33, v101
	s_nop 1
	v_mov_b32_dpp v128, v126 quad_perm:[1,0,3,2] row_mask:0xf bank_mask:0xf
	v_mov_b32_dpp v129, v127 quad_perm:[1,0,3,2] row_mask:0xf bank_mask:0xf
	v_cndmask_b32_e64 v130, v126, v129, s[100:101]
	v_cndmask_b32_e64 v131, v128, v127, s[100:101]
	v_cvt_pk_bf16_f32 v130, v130, v131
	global_store_dword v[120:121], v130, off offset:128
	v_mul_f32_e32 v126, v16, v100
	v_mul_f32_e32 v127, v17, v101
	s_nop 1
	v_mov_b32_dpp v128, v126 quad_perm:[1,0,3,2] row_mask:0xf bank_mask:0xf
	v_mov_b32_dpp v129, v127 quad_perm:[1,0,3,2] row_mask:0xf bank_mask:0xf
	v_cndmask_b32_e64 v130, v126, v129, s[100:101]
	v_cndmask_b32_e64 v131, v128, v127, s[100:101]
	v_cvt_pk_bf16_f32 v130, v130, v131
	global_store_dword v[120:121], v130, off offset:192
	v_mov_b32_e32 v124, 0x2000
	v_lshl_add_u64 v[122:123], v[120:121], 0, v[124:125]
	v_mul_f32_e32 v126, v2, v102
	v_mul_f32_e32 v127, v3, v103
	s_nop 1
	v_mov_b32_dpp v128, v126 quad_perm:[1,0,3,2] row_mask:0xf bank_mask:0xf
	v_mov_b32_dpp v129, v127 quad_perm:[1,0,3,2] row_mask:0xf bank_mask:0xf
	v_cndmask_b32_e64 v130, v126, v129, s[100:101]
	v_cndmask_b32_e64 v131, v128, v127, s[100:101]
	v_cvt_pk_bf16_f32 v130, v130, v131
	global_store_dword v[122:123], v130, off
	v_mul_f32_e32 v126, v50, v102
	v_mul_f32_e32 v127, v51, v103
	s_nop 1
	v_mov_b32_dpp v128, v126 quad_perm:[1,0,3,2] row_mask:0xf bank_mask:0xf
	v_mov_b32_dpp v129, v127 quad_perm:[1,0,3,2] row_mask:0xf bank_mask:0xf
	v_cndmask_b32_e64 v130, v126, v129, s[100:101]
	v_cndmask_b32_e64 v131, v128, v127, s[100:101]
	v_cvt_pk_bf16_f32 v130, v130, v131
	global_store_dword v[122:123], v130, off offset:64
	v_mul_f32_e32 v126, v34, v102
	v_mul_f32_e32 v127, v35, v103
	s_nop 1
	v_mov_b32_dpp v128, v126 quad_perm:[1,0,3,2] row_mask:0xf bank_mask:0xf
	v_mov_b32_dpp v129, v127 quad_perm:[1,0,3,2] row_mask:0xf bank_mask:0xf
	v_cndmask_b32_e64 v130, v126, v129, s[100:101]
	v_cndmask_b32_e64 v131, v128, v127, s[100:101]
	v_cvt_pk_bf16_f32 v130, v130, v131
	global_store_dword v[122:123], v130, off offset:128
	v_mul_f32_e32 v126, v18, v102
	v_mul_f32_e32 v127, v19, v103
	s_nop 1
	v_mov_b32_dpp v128, v126 quad_perm:[1,0,3,2] row_mask:0xf bank_mask:0xf
	v_mov_b32_dpp v129, v127 quad_perm:[1,0,3,2] row_mask:0xf bank_mask:0xf
	v_cndmask_b32_e64 v130, v126, v129, s[100:101]
	v_cndmask_b32_e64 v131, v128, v127, s[100:101]
	v_cvt_pk_bf16_f32 v130, v130, v131
	global_store_dword v[122:123], v130, off offset:192
	v_mov_b32_e32 v124, 0x8000
	v_lshl_add_u64 v[122:123], v[120:121], 0, v[124:125]
	v_mul_f32_e32 v126, v4, v104
	v_mul_f32_e32 v127, v5, v105
	s_nop 1
	v_mov_b32_dpp v128, v126 quad_perm:[1,0,3,2] row_mask:0xf bank_mask:0xf
	v_mov_b32_dpp v129, v127 quad_perm:[1,0,3,2] row_mask:0xf bank_mask:0xf
	v_cndmask_b32_e64 v130, v126, v129, s[100:101]
	v_cndmask_b32_e64 v131, v128, v127, s[100:101]
	v_cvt_pk_bf16_f32 v130, v130, v131
	global_store_dword v[122:123], v130, off
	v_mul_f32_e32 v126, v52, v104
	v_mul_f32_e32 v127, v53, v105
	s_nop 1
	v_mov_b32_dpp v128, v126 quad_perm:[1,0,3,2] row_mask:0xf bank_mask:0xf
	v_mov_b32_dpp v129, v127 quad_perm:[1,0,3,2] row_mask:0xf bank_mask:0xf
	v_cndmask_b32_e64 v130, v126, v129, s[100:101]
	v_cndmask_b32_e64 v131, v128, v127, s[100:101]
	v_cvt_pk_bf16_f32 v130, v130, v131
	global_store_dword v[122:123], v130, off offset:64
	v_mul_f32_e32 v126, v36, v104
	v_mul_f32_e32 v127, v37, v105
	s_nop 1
	v_mov_b32_dpp v128, v126 quad_perm:[1,0,3,2] row_mask:0xf bank_mask:0xf
	v_mov_b32_dpp v129, v127 quad_perm:[1,0,3,2] row_mask:0xf bank_mask:0xf
	v_cndmask_b32_e64 v130, v126, v129, s[100:101]
	v_cndmask_b32_e64 v131, v128, v127, s[100:101]
	v_cvt_pk_bf16_f32 v130, v130, v131
	global_store_dword v[122:123], v130, off offset:128
	v_mul_f32_e32 v126, v20, v104
	v_mul_f32_e32 v127, v21, v105
	s_nop 1
	v_mov_b32_dpp v128, v126 quad_perm:[1,0,3,2] row_mask:0xf bank_mask:0xf
	v_mov_b32_dpp v129, v127 quad_perm:[1,0,3,2] row_mask:0xf bank_mask:0xf
	v_cndmask_b32_e64 v130, v126, v129, s[100:101]
	v_cndmask_b32_e64 v131, v128, v127, s[100:101]
	v_cvt_pk_bf16_f32 v130, v130, v131
	global_store_dword v[122:123], v130, off offset:192
	v_mov_b32_e32 v124, 0xa000
	v_lshl_add_u64 v[122:123], v[120:121], 0, v[124:125]
	v_mul_f32_e32 v126, v6, v106
	v_mul_f32_e32 v127, v7, v107
	s_nop 1
	v_mov_b32_dpp v128, v126 quad_perm:[1,0,3,2] row_mask:0xf bank_mask:0xf
	v_mov_b32_dpp v129, v127 quad_perm:[1,0,3,2] row_mask:0xf bank_mask:0xf
	v_cndmask_b32_e64 v130, v126, v129, s[100:101]
	v_cndmask_b32_e64 v131, v128, v127, s[100:101]
	v_cvt_pk_bf16_f32 v130, v130, v131
	global_store_dword v[122:123], v130, off
	v_mul_f32_e32 v126, v54, v106
	v_mul_f32_e32 v127, v55, v107
	s_nop 1
	v_mov_b32_dpp v128, v126 quad_perm:[1,0,3,2] row_mask:0xf bank_mask:0xf
	v_mov_b32_dpp v129, v127 quad_perm:[1,0,3,2] row_mask:0xf bank_mask:0xf
	v_cndmask_b32_e64 v130, v126, v129, s[100:101]
	v_cndmask_b32_e64 v131, v128, v127, s[100:101]
	v_cvt_pk_bf16_f32 v130, v130, v131
	global_store_dword v[122:123], v130, off offset:64
	v_mul_f32_e32 v126, v38, v106
	v_mul_f32_e32 v127, v39, v107
	s_nop 1
	v_mov_b32_dpp v128, v126 quad_perm:[1,0,3,2] row_mask:0xf bank_mask:0xf
	v_mov_b32_dpp v129, v127 quad_perm:[1,0,3,2] row_mask:0xf bank_mask:0xf
	v_cndmask_b32_e64 v130, v126, v129, s[100:101]
	v_cndmask_b32_e64 v131, v128, v127, s[100:101]
	v_cvt_pk_bf16_f32 v130, v130, v131
	global_store_dword v[122:123], v130, off offset:128
	v_mul_f32_e32 v126, v22, v106
	v_mul_f32_e32 v127, v23, v107
	s_nop 1
	v_mov_b32_dpp v128, v126 quad_perm:[1,0,3,2] row_mask:0xf bank_mask:0xf
	v_mov_b32_dpp v129, v127 quad_perm:[1,0,3,2] row_mask:0xf bank_mask:0xf
	v_cndmask_b32_e64 v130, v126, v129, s[100:101]
	v_cndmask_b32_e64 v131, v128, v127, s[100:101]
	v_cvt_pk_bf16_f32 v130, v130, v131
	global_store_dword v[122:123], v130, off offset:192
	v_mov_b32_e32 v124, 0x10000
	v_lshl_add_u64 v[122:123], v[120:121], 0, v[124:125]
	v_mul_f32_e32 v126, v8, v108
	v_mul_f32_e32 v127, v9, v109
	s_nop 1
	v_mov_b32_dpp v128, v126 quad_perm:[1,0,3,2] row_mask:0xf bank_mask:0xf
	v_mov_b32_dpp v129, v127 quad_perm:[1,0,3,2] row_mask:0xf bank_mask:0xf
	v_cndmask_b32_e64 v130, v126, v129, s[100:101]
	v_cndmask_b32_e64 v131, v128, v127, s[100:101]
	v_cvt_pk_bf16_f32 v130, v130, v131
	global_store_dword v[122:123], v130, off
	v_mul_f32_e32 v126, v56, v108
	v_mul_f32_e32 v127, v57, v109
	s_nop 1
	v_mov_b32_dpp v128, v126 quad_perm:[1,0,3,2] row_mask:0xf bank_mask:0xf
	v_mov_b32_dpp v129, v127 quad_perm:[1,0,3,2] row_mask:0xf bank_mask:0xf
	v_cndmask_b32_e64 v130, v126, v129, s[100:101]
	v_cndmask_b32_e64 v131, v128, v127, s[100:101]
	v_cvt_pk_bf16_f32 v130, v130, v131
	global_store_dword v[122:123], v130, off offset:64
	v_mul_f32_e32 v126, v40, v108
	v_mul_f32_e32 v127, v41, v109
	s_nop 1
	v_mov_b32_dpp v128, v126 quad_perm:[1,0,3,2] row_mask:0xf bank_mask:0xf
	v_mov_b32_dpp v129, v127 quad_perm:[1,0,3,2] row_mask:0xf bank_mask:0xf
	v_cndmask_b32_e64 v130, v126, v129, s[100:101]
	v_cndmask_b32_e64 v131, v128, v127, s[100:101]
	v_cvt_pk_bf16_f32 v130, v130, v131
	global_store_dword v[122:123], v130, off offset:128
	v_mul_f32_e32 v126, v24, v108
	v_mul_f32_e32 v127, v25, v109
	s_nop 1
	v_mov_b32_dpp v128, v126 quad_perm:[1,0,3,2] row_mask:0xf bank_mask:0xf
	v_mov_b32_dpp v129, v127 quad_perm:[1,0,3,2] row_mask:0xf bank_mask:0xf
	v_cndmask_b32_e64 v130, v126, v129, s[100:101]
	v_cndmask_b32_e64 v131, v128, v127, s[100:101]
	v_cvt_pk_bf16_f32 v130, v130, v131
	global_store_dword v[122:123], v130, off offset:192
	v_mov_b32_e32 v124, 0x12000
	v_lshl_add_u64 v[122:123], v[120:121], 0, v[124:125]
	v_mul_f32_e32 v126, v10, v110
	v_mul_f32_e32 v127, v11, v111
	s_nop 1
	v_mov_b32_dpp v128, v126 quad_perm:[1,0,3,2] row_mask:0xf bank_mask:0xf
	v_mov_b32_dpp v129, v127 quad_perm:[1,0,3,2] row_mask:0xf bank_mask:0xf
	v_cndmask_b32_e64 v130, v126, v129, s[100:101]
	v_cndmask_b32_e64 v131, v128, v127, s[100:101]
	v_cvt_pk_bf16_f32 v130, v130, v131
	global_store_dword v[122:123], v130, off
	v_mul_f32_e32 v126, v58, v110
	v_mul_f32_e32 v127, v59, v111
	s_nop 1
	v_mov_b32_dpp v128, v126 quad_perm:[1,0,3,2] row_mask:0xf bank_mask:0xf
	v_mov_b32_dpp v129, v127 quad_perm:[1,0,3,2] row_mask:0xf bank_mask:0xf
	v_cndmask_b32_e64 v130, v126, v129, s[100:101]
	v_cndmask_b32_e64 v131, v128, v127, s[100:101]
	v_cvt_pk_bf16_f32 v130, v130, v131
	global_store_dword v[122:123], v130, off offset:64
	v_mul_f32_e32 v126, v42, v110
	v_mul_f32_e32 v127, v43, v111
	s_nop 1
	v_mov_b32_dpp v128, v126 quad_perm:[1,0,3,2] row_mask:0xf bank_mask:0xf
	v_mov_b32_dpp v129, v127 quad_perm:[1,0,3,2] row_mask:0xf bank_mask:0xf
	v_cndmask_b32_e64 v130, v126, v129, s[100:101]
	v_cndmask_b32_e64 v131, v128, v127, s[100:101]
	v_cvt_pk_bf16_f32 v130, v130, v131
	global_store_dword v[122:123], v130, off offset:128
	v_mul_f32_e32 v126, v26, v110
	v_mul_f32_e32 v127, v27, v111
	s_nop 1
	v_mov_b32_dpp v128, v126 quad_perm:[1,0,3,2] row_mask:0xf bank_mask:0xf
	v_mov_b32_dpp v129, v127 quad_perm:[1,0,3,2] row_mask:0xf bank_mask:0xf
	v_cndmask_b32_e64 v130, v126, v129, s[100:101]
	v_cndmask_b32_e64 v131, v128, v127, s[100:101]
	v_cvt_pk_bf16_f32 v130, v130, v131
	global_store_dword v[122:123], v130, off offset:192
	v_mov_b32_e32 v124, 0x18000
	v_lshl_add_u64 v[122:123], v[120:121], 0, v[124:125]
	v_mul_f32_e32 v126, v12, v112
	v_mul_f32_e32 v127, v13, v113
	s_nop 1
	v_mov_b32_dpp v128, v126 quad_perm:[1,0,3,2] row_mask:0xf bank_mask:0xf
	v_mov_b32_dpp v129, v127 quad_perm:[1,0,3,2] row_mask:0xf bank_mask:0xf
	v_cndmask_b32_e64 v130, v126, v129, s[100:101]
	v_cndmask_b32_e64 v131, v128, v127, s[100:101]
	v_cvt_pk_bf16_f32 v130, v130, v131
	global_store_dword v[122:123], v130, off
	v_mul_f32_e32 v126, v60, v112
	v_mul_f32_e32 v127, v61, v113
	s_nop 1
	v_mov_b32_dpp v128, v126 quad_perm:[1,0,3,2] row_mask:0xf bank_mask:0xf
	v_mov_b32_dpp v129, v127 quad_perm:[1,0,3,2] row_mask:0xf bank_mask:0xf
	v_cndmask_b32_e64 v130, v126, v129, s[100:101]
	v_cndmask_b32_e64 v131, v128, v127, s[100:101]
	v_cvt_pk_bf16_f32 v130, v130, v131
	global_store_dword v[122:123], v130, off offset:64
	v_mul_f32_e32 v126, v44, v112
	v_mul_f32_e32 v127, v45, v113
	s_nop 1
	v_mov_b32_dpp v128, v126 quad_perm:[1,0,3,2] row_mask:0xf bank_mask:0xf
	v_mov_b32_dpp v129, v127 quad_perm:[1,0,3,2] row_mask:0xf bank_mask:0xf
	v_cndmask_b32_e64 v130, v126, v129, s[100:101]
	v_cndmask_b32_e64 v131, v128, v127, s[100:101]
	v_cvt_pk_bf16_f32 v130, v130, v131
	global_store_dword v[122:123], v130, off offset:128
	v_mul_f32_e32 v126, v28, v112
	v_mul_f32_e32 v127, v29, v113
	s_nop 1
	v_mov_b32_dpp v128, v126 quad_perm:[1,0,3,2] row_mask:0xf bank_mask:0xf
	v_mov_b32_dpp v129, v127 quad_perm:[1,0,3,2] row_mask:0xf bank_mask:0xf
	v_cndmask_b32_e64 v130, v126, v129, s[100:101]
	v_cndmask_b32_e64 v131, v128, v127, s[100:101]
	v_cvt_pk_bf16_f32 v130, v130, v131
	global_store_dword v[122:123], v130, off offset:192
	v_mov_b32_e32 v124, 0x1a000
	v_lshl_add_u64 v[122:123], v[120:121], 0, v[124:125]
	v_mul_f32_e32 v126, v14, v114
	v_mul_f32_e32 v127, v15, v115
	s_nop 1
	v_mov_b32_dpp v128, v126 quad_perm:[1,0,3,2] row_mask:0xf bank_mask:0xf
	v_mov_b32_dpp v129, v127 quad_perm:[1,0,3,2] row_mask:0xf bank_mask:0xf
	v_cndmask_b32_e64 v130, v126, v129, s[100:101]
	v_cndmask_b32_e64 v131, v128, v127, s[100:101]
	v_cvt_pk_bf16_f32 v130, v130, v131
	global_store_dword v[122:123], v130, off
	v_mul_f32_e32 v126, v62, v114
	v_mul_f32_e32 v127, v63, v115
	s_nop 1
	v_mov_b32_dpp v128, v126 quad_perm:[1,0,3,2] row_mask:0xf bank_mask:0xf
	v_mov_b32_dpp v129, v127 quad_perm:[1,0,3,2] row_mask:0xf bank_mask:0xf
	v_cndmask_b32_e64 v130, v126, v129, s[100:101]
	v_cndmask_b32_e64 v131, v128, v127, s[100:101]
	v_cvt_pk_bf16_f32 v130, v130, v131
	global_store_dword v[122:123], v130, off offset:64
	v_mul_f32_e32 v126, v46, v114
	v_mul_f32_e32 v127, v47, v115
	s_nop 1
	v_mov_b32_dpp v128, v126 quad_perm:[1,0,3,2] row_mask:0xf bank_mask:0xf
	v_mov_b32_dpp v129, v127 quad_perm:[1,0,3,2] row_mask:0xf bank_mask:0xf
	v_cndmask_b32_e64 v130, v126, v129, s[100:101]
	v_cndmask_b32_e64 v131, v128, v127, s[100:101]
	v_cvt_pk_bf16_f32 v130, v130, v131
	global_store_dword v[122:123], v130, off offset:128
	v_mul_f32_e32 v126, v30, v114
	v_mul_f32_e32 v127, v31, v115
	s_nop 1
	v_mov_b32_dpp v128, v126 quad_perm:[1,0,3,2] row_mask:0xf bank_mask:0xf
	v_mov_b32_dpp v129, v127 quad_perm:[1,0,3,2] row_mask:0xf bank_mask:0xf
	v_cndmask_b32_e64 v130, v126, v129, s[100:101]
	v_cndmask_b32_e64 v131, v128, v127, s[100:101]
	v_cvt_pk_bf16_f32 v130, v130, v131
	global_store_dword v[122:123], v130, off offset:192
	v_readlane_b32 s0, v254, 47
	v_readlane_b32 s1, v255, 9
	s_add_i32 s1, s1, s0
	s_cmpk_gt_i32 s1, 0x17f
	s_waitcnt vmcnt(63) expcnt(7) lgkmcnt(15)
	s_barrier
	s_cbranch_scc1 .LBB0_631

.LBB0_633:
	s_or_b64 exec, exec, s[0:1]
	s_waitcnt lgkmcnt(0)
	v_add_u32_e32 v72, v151, v150
	ds_read_b128 v[64:67], v72
	ds_read_b128 v[68:71], v72 offset:32
	s_lshl_b64 s[0:1], s[4:5], 12
	v_readlane_b32 s2, v254, 42
	s_add_u32 s0, s2, s0
	s_waitcnt lgkmcnt(1)
	v_rcp_f32_e32 v73, v64
	v_rcp_f32_e32 v74, v65
	v_rcp_f32_e32 v75, v66
	v_rcp_f32_e32 v76, v67
	ds_read_b128 v[64:67], v72 offset:64
	v_readlane_b32 s2, v254, 44
	s_addc_u32 s1, s2, s1
	s_add_u32 s0, s0, s6
	v_ashrrev_i32_e32 v149, 31, v148
	s_addc_u32 s1, s1, s7
	s_waitcnt lgkmcnt(1)
	v_rcp_f32_e32 v77, v68
	v_rcp_f32_e32 v78, v69
	v_rcp_f32_e32 v79, v70
	v_rcp_f32_e32 v80, v71
	ds_read_b128 v[68:71], v72 offset:96
	s_waitcnt lgkmcnt(1)
	v_rcp_f32_e32 v72, v64
	v_rcp_f32_e32 v81, v65
	v_lshlrev_b64 v[64:65], 12, v[148:149]
	v_lshl_add_u64 v[64:65], s[0:1], 0, v[64:65]
	v_lshlrev_b32_e32 v192, 1, v154
	v_rcp_f32_e32 v82, v66
	v_rcp_f32_e32 v83, v67
	v_lshlrev_b32_e32 v66, 14, v155
	v_lshl_add_u64 v[64:65], v[64:65], 0, v[192:193]
	v_mov_b32_e32 v67, v193
	v_lshl_add_u64 v[64:65], v[64:65], 0, v[66:67]
	s_movk_i32 s1, 0x7fff
	v_add_u32_e32 v116, v151, v150
	ds_read_b128 v[100:103], v116
	ds_read_b128 v[104:107], v116 offset:32
	ds_read_b128 v[108:111], v116 offset:64
	ds_read_b128 v[112:115], v116 offset:96
	v_and_b32_e32 v117, 1, v154
	v_cmp_eq_u32_e64 s[100:101], 1, v117
	v_mov_b32_e32 v118, 0xffe
	v_cndmask_b32_e64 v118, 0, v118, s[100:101]
	v_mov_b32_e32 v119, 0
	v_lshl_add_u64 v[120:121], v[64:65], 0, v[118:119]
	v_mov_b32_e32 v125, 0
	s_waitcnt lgkmcnt(0)
	v_rcp_f32_e32 v100, v100
	v_rcp_f32_e32 v101, v101
	v_rcp_f32_e32 v102, v102
	v_rcp_f32_e32 v103, v103
	v_rcp_f32_e32 v104, v104
	v_rcp_f32_e32 v105, v105
	v_rcp_f32_e32 v106, v106
	v_rcp_f32_e32 v107, v107
	v_rcp_f32_e32 v108, v108
	v_rcp_f32_e32 v109, v109
	v_rcp_f32_e32 v110, v110
	v_rcp_f32_e32 v111, v111
	v_rcp_f32_e32 v112, v112
	v_rcp_f32_e32 v113, v113
	v_rcp_f32_e32 v114, v114
	v_rcp_f32_e32 v115, v115
	v_mul_f32_e32 v126, v48, v100
	v_mul_f32_e32 v127, v49, v101
	s_nop 1
	v_mov_b32_dpp v128, v126 quad_perm:[1,0,3,2] row_mask:0xf bank_mask:0xf
	v_mov_b32_dpp v129, v127 quad_perm:[1,0,3,2] row_mask:0xf bank_mask:0xf
	v_cndmask_b32_e64 v130, v126, v129, s[100:101]
	v_cndmask_b32_e64 v131, v128, v127, s[100:101]
	v_cvt_pk_bf16_f32 v130, v130, v131
	global_store_dword v[120:121], v130, off offset:3072
	v_mul_f32_e32 v126, v32, v100
	v_mul_f32_e32 v127, v33, v101
	s_nop 1
	v_mov_b32_dpp v128, v126 quad_perm:[1,0,3,2] row_mask:0xf bank_mask:0xf
	v_mov_b32_dpp v129, v127 quad_perm:[1,0,3,2] row_mask:0xf bank_mask:0xf
	v_cndmask_b32_e64 v130, v126, v129, s[100:101]
	v_cndmask_b32_e64 v131, v128, v127, s[100:101]
	v_cvt_pk_bf16_f32 v130, v130, v131
	global_store_dword v[120:121], v130, off offset:3136
	v_mul_f32_e32 v126, v16, v100
	v_mul_f32_e32 v127, v17, v101
	s_nop 1
	v_mov_b32_dpp v128, v126 quad_perm:[1,0,3,2] row_mask:0xf bank_mask:0xf
	v_mov_b32_dpp v129, v127 quad_perm:[1,0,3,2] row_mask:0xf bank_mask:0xf
	v_cndmask_b32_e64 v130, v126, v129, s[100:101]
	v_cndmask_b32_e64 v131, v128, v127, s[100:101]
	v_cvt_pk_bf16_f32 v130, v130, v131
	global_store_dword v[120:121], v130, off offset:3200
	v_mul_f32_e32 v126, v0, v100
	v_mul_f32_e32 v127, v1, v101
	s_nop 1
	v_mov_b32_dpp v128, v126 quad_perm:[1,0,3,2] row_mask:0xf bank_mask:0xf
	v_mov_b32_dpp v129, v127 quad_perm:[1,0,3,2] row_mask:0xf bank_mask:0xf
	v_cndmask_b32_e64 v130, v126, v129, s[100:101]
	v_cndmask_b32_e64 v131, v128, v127, s[100:101]
	v_cvt_pk_bf16_f32 v130, v130, v131
	global_store_dword v[120:121], v130, off offset:3264
	v_mov_b32_e32 v124, 0x2000
	v_lshl_add_u64 v[122:123], v[120:121], 0, v[124:125]
	v_mul_f32_e32 v126, v50, v102
	v_mul_f32_e32 v127, v51, v103
	s_nop 1
	v_mov_b32_dpp v128, v126 quad_perm:[1,0,3,2] row_mask:0xf bank_mask:0xf
	v_mov_b32_dpp v129, v127 quad_perm:[1,0,3,2] row_mask:0xf bank_mask:0xf
	v_cndmask_b32_e64 v130, v126, v129, s[100:101]
	v_cndmask_b32_e64 v131, v128, v127, s[100:101]
	v_cvt_pk_bf16_f32 v130, v130, v131
	global_store_dword v[122:123], v130, off offset:3072
	v_mul_f32_e32 v126, v34, v102
	v_mul_f32_e32 v127, v35, v103
	s_nop 1
	v_mov_b32_dpp v128, v126 quad_perm:[1,0,3,2] row_mask:0xf bank_mask:0xf
	v_mov_b32_dpp v129, v127 quad_perm:[1,0,3,2] row_mask:0xf bank_mask:0xf
	v_cndmask_b32_e64 v130, v126, v129, s[100:101]
	v_cndmask_b32_e64 v131, v128, v127, s[100:101]
	v_cvt_pk_bf16_f32 v130, v130, v131
	global_store_dword v[122:123], v130, off offset:3136
	v_mul_f32_e32 v126, v18, v102
	v_mul_f32_e32 v127, v19, v103
	s_nop 1
	v_mov_b32_dpp v128, v126 quad_perm:[1,0,3,2] row_mask:0xf bank_mask:0xf
	v_mov_b32_dpp v129, v127 quad_perm:[1,0,3,2] row_mask:0xf bank_mask:0xf
	v_cndmask_b32_e64 v130, v126, v129, s[100:101]
	v_cndmask_b32_e64 v131, v128, v127, s[100:101]
	v_cvt_pk_bf16_f32 v130, v130, v131
	global_store_dword v[122:123], v130, off offset:3200
	v_mul_f32_e32 v126, v2, v102
	v_mul_f32_e32 v127, v3, v103
	s_nop 1
	v_mov_b32_dpp v128, v126 quad_perm:[1,0,3,2] row_mask:0xf bank_mask:0xf
	v_mov_b32_dpp v129, v127 quad_perm:[1,0,3,2] row_mask:0xf bank_mask:0xf
	v_cndmask_b32_e64 v130, v126, v129, s[100:101]
	v_cndmask_b32_e64 v131, v128, v127, s[100:101]
	v_cvt_pk_bf16_f32 v130, v130, v131
	global_store_dword v[122:123], v130, off offset:3264
	v_mov_b32_e32 v124, 0x8000
	v_lshl_add_u64 v[122:123], v[120:121], 0, v[124:125]
	v_mul_f32_e32 v126, v52, v104
	v_mul_f32_e32 v127, v53, v105
	s_nop 1
	v_mov_b32_dpp v128, v126 quad_perm:[1,0,3,2] row_mask:0xf bank_mask:0xf
	v_mov_b32_dpp v129, v127 quad_perm:[1,0,3,2] row_mask:0xf bank_mask:0xf
	v_cndmask_b32_e64 v130, v126, v129, s[100:101]
	v_cndmask_b32_e64 v131, v128, v127, s[100:101]
	v_cvt_pk_bf16_f32 v130, v130, v131
	global_store_dword v[122:123], v130, off offset:3072
	v_mul_f32_e32 v126, v36, v104
	v_mul_f32_e32 v127, v37, v105
	s_nop 1
	v_mov_b32_dpp v128, v126 quad_perm:[1,0,3,2] row_mask:0xf bank_mask:0xf
	v_mov_b32_dpp v129, v127 quad_perm:[1,0,3,2] row_mask:0xf bank_mask:0xf
	v_cndmask_b32_e64 v130, v126, v129, s[100:101]
	v_cndmask_b32_e64 v131, v128, v127, s[100:101]
	v_cvt_pk_bf16_f32 v130, v130, v131
	global_store_dword v[122:123], v130, off offset:3136
	v_mul_f32_e32 v126, v20, v104
	v_mul_f32_e32 v127, v21, v105
	s_nop 1
	v_mov_b32_dpp v128, v126 quad_perm:[1,0,3,2] row_mask:0xf bank_mask:0xf
	v_mov_b32_dpp v129, v127 quad_perm:[1,0,3,2] row_mask:0xf bank_mask:0xf
	v_cndmask_b32_e64 v130, v126, v129, s[100:101]
	v_cndmask_b32_e64 v131, v128, v127, s[100:101]
	v_cvt_pk_bf16_f32 v130, v130, v131
	global_store_dword v[122:123], v130, off offset:3200
	v_mul_f32_e32 v126, v4, v104
	v_mul_f32_e32 v127, v5, v105
	s_nop 1
	v_mov_b32_dpp v128, v126 quad_perm:[1,0,3,2] row_mask:0xf bank_mask:0xf
	v_mov_b32_dpp v129, v127 quad_perm:[1,0,3,2] row_mask:0xf bank_mask:0xf
	v_cndmask_b32_e64 v130, v126, v129, s[100:101]
	v_cndmask_b32_e64 v131, v128, v127, s[100:101]
	v_cvt_pk_bf16_f32 v130, v130, v131
	global_store_dword v[122:123], v130, off offset:3264
	v_mov_b32_e32 v124, 0xa000
	v_lshl_add_u64 v[122:123], v[120:121], 0, v[124:125]
	v_mul_f32_e32 v126, v54, v106
	v_mul_f32_e32 v127, v55, v107
	s_nop 1
	v_mov_b32_dpp v128, v126 quad_perm:[1,0,3,2] row_mask:0xf bank_mask:0xf
	v_mov_b32_dpp v129, v127 quad_perm:[1,0,3,2] row_mask:0xf bank_mask:0xf
	v_cndmask_b32_e64 v130, v126, v129, s[100:101]
	v_cndmask_b32_e64 v131, v128, v127, s[100:101]
	v_cvt_pk_bf16_f32 v130, v130, v131
	global_store_dword v[122:123], v130, off offset:3072
	v_mul_f32_e32 v126, v38, v106
	v_mul_f32_e32 v127, v39, v107
	s_nop 1
	v_mov_b32_dpp v128, v126 quad_perm:[1,0,3,2] row_mask:0xf bank_mask:0xf
	v_mov_b32_dpp v129, v127 quad_perm:[1,0,3,2] row_mask:0xf bank_mask:0xf
	v_cndmask_b32_e64 v130, v126, v129, s[100:101]
	v_cndmask_b32_e64 v131, v128, v127, s[100:101]
	v_cvt_pk_bf16_f32 v130, v130, v131
	global_store_dword v[122:123], v130, off offset:3136
	v_mul_f32_e32 v126, v22, v106
	v_mul_f32_e32 v127, v23, v107
	s_nop 1
	v_mov_b32_dpp v128, v126 quad_perm:[1,0,3,2] row_mask:0xf bank_mask:0xf
	v_mov_b32_dpp v129, v127 quad_perm:[1,0,3,2] row_mask:0xf bank_mask:0xf
	v_cndmask_b32_e64 v130, v126, v129, s[100:101]
	v_cndmask_b32_e64 v131, v128, v127, s[100:101]
	v_cvt_pk_bf16_f32 v130, v130, v131
	global_store_dword v[122:123], v130, off offset:3200
	v_mul_f32_e32 v126, v6, v106
	v_mul_f32_e32 v127, v7, v107
	s_nop 1
	v_mov_b32_dpp v128, v126 quad_perm:[1,0,3,2] row_mask:0xf bank_mask:0xf
	v_mov_b32_dpp v129, v127 quad_perm:[1,0,3,2] row_mask:0xf bank_mask:0xf
	v_cndmask_b32_e64 v130, v126, v129, s[100:101]
	v_cndmask_b32_e64 v131, v128, v127, s[100:101]
	v_cvt_pk_bf16_f32 v130, v130, v131
	global_store_dword v[122:123], v130, off offset:3264
	v_mov_b32_e32 v124, 0x10000
	v_lshl_add_u64 v[122:123], v[120:121], 0, v[124:125]
	v_mul_f32_e32 v126, v56, v108
	v_mul_f32_e32 v127, v57, v109
	s_nop 1
	v_mov_b32_dpp v128, v126 quad_perm:[1,0,3,2] row_mask:0xf bank_mask:0xf
	v_mov_b32_dpp v129, v127 quad_perm:[1,0,3,2] row_mask:0xf bank_mask:0xf
	v_cndmask_b32_e64 v130, v126, v129, s[100:101]
	v_cndmask_b32_e64 v131, v128, v127, s[100:101]
	v_cvt_pk_bf16_f32 v130, v130, v131
	global_store_dword v[122:123], v130, off offset:3072
	v_mul_f32_e32 v126, v40, v108
	v_mul_f32_e32 v127, v41, v109
	s_nop 1
	v_mov_b32_dpp v128, v126 quad_perm:[1,0,3,2] row_mask:0xf bank_mask:0xf
	v_mov_b32_dpp v129, v127 quad_perm:[1,0,3,2] row_mask:0xf bank_mask:0xf
	v_cndmask_b32_e64 v130, v126, v129, s[100:101]
	v_cndmask_b32_e64 v131, v128, v127, s[100:101]
	v_cvt_pk_bf16_f32 v130, v130, v131
	global_store_dword v[122:123], v130, off offset:3136
	v_mul_f32_e32 v126, v24, v108
	v_mul_f32_e32 v127, v25, v109
	s_nop 1
	v_mov_b32_dpp v128, v126 quad_perm:[1,0,3,2] row_mask:0xf bank_mask:0xf
	v_mov_b32_dpp v129, v127 quad_perm:[1,0,3,2] row_mask:0xf bank_mask:0xf
	v_cndmask_b32_e64 v130, v126, v129, s[100:101]
	v_cndmask_b32_e64 v131, v128, v127, s[100:101]
	v_cvt_pk_bf16_f32 v130, v130, v131
	global_store_dword v[122:123], v130, off offset:3200
	v_mul_f32_e32 v126, v8, v108
	v_mul_f32_e32 v127, v9, v109
	s_nop 1
	v_mov_b32_dpp v128, v126 quad_perm:[1,0,3,2] row_mask:0xf bank_mask:0xf
	v_mov_b32_dpp v129, v127 quad_perm:[1,0,3,2] row_mask:0xf bank_mask:0xf
	v_cndmask_b32_e64 v130, v126, v129, s[100:101]
	v_cndmask_b32_e64 v131, v128, v127, s[100:101]
	v_cvt_pk_bf16_f32 v130, v130, v131
	global_store_dword v[122:123], v130, off offset:3264
	v_mov_b32_e32 v124, 0x12000
	v_lshl_add_u64 v[122:123], v[120:121], 0, v[124:125]
	v_mul_f32_e32 v126, v58, v110
	v_mul_f32_e32 v127, v59, v111
	s_nop 1
	v_mov_b32_dpp v128, v126 quad_perm:[1,0,3,2] row_mask:0xf bank_mask:0xf
	v_mov_b32_dpp v129, v127 quad_perm:[1,0,3,2] row_mask:0xf bank_mask:0xf
	v_cndmask_b32_e64 v130, v126, v129, s[100:101]
	v_cndmask_b32_e64 v131, v128, v127, s[100:101]
	v_cvt_pk_bf16_f32 v130, v130, v131
	global_store_dword v[122:123], v130, off offset:3072
	v_mul_f32_e32 v126, v42, v110
	v_mul_f32_e32 v127, v43, v111
	s_nop 1
	v_mov_b32_dpp v128, v126 quad_perm:[1,0,3,2] row_mask:0xf bank_mask:0xf
	v_mov_b32_dpp v129, v127 quad_perm:[1,0,3,2] row_mask:0xf bank_mask:0xf
	v_cndmask_b32_e64 v130, v126, v129, s[100:101]
	v_cndmask_b32_e64 v131, v128, v127, s[100:101]
	v_cvt_pk_bf16_f32 v130, v130, v131
	global_store_dword v[122:123], v130, off offset:3136
	v_mul_f32_e32 v126, v26, v110
	v_mul_f32_e32 v127, v27, v111
	s_nop 1
	v_mov_b32_dpp v128, v126 quad_perm:[1,0,3,2] row_mask:0xf bank_mask:0xf
	v_mov_b32_dpp v129, v127 quad_perm:[1,0,3,2] row_mask:0xf bank_mask:0xf
	v_cndmask_b32_e64 v130, v126, v129, s[100:101]
	v_cndmask_b32_e64 v131, v128, v127, s[100:101]
	v_cvt_pk_bf16_f32 v130, v130, v131
	global_store_dword v[122:123], v130, off offset:3200
	v_mul_f32_e32 v126, v10, v110
	v_mul_f32_e32 v127, v11, v111
	s_nop 1
	v_mov_b32_dpp v128, v126 quad_perm:[1,0,3,2] row_mask:0xf bank_mask:0xf
	v_mov_b32_dpp v129, v127 quad_perm:[1,0,3,2] row_mask:0xf bank_mask:0xf
	v_cndmask_b32_e64 v130, v126, v129, s[100:101]
	v_cndmask_b32_e64 v131, v128, v127, s[100:101]
	v_cvt_pk_bf16_f32 v130, v130, v131
	global_store_dword v[122:123], v130, off offset:3264
	v_mov_b32_e32 v124, 0x18000
	v_lshl_add_u64 v[122:123], v[120:121], 0, v[124:125]
	v_mul_f32_e32 v126, v60, v112
	v_mul_f32_e32 v127, v61, v113
	s_nop 1
	v_mov_b32_dpp v128, v126 quad_perm:[1,0,3,2] row_mask:0xf bank_mask:0xf
	v_mov_b32_dpp v129, v127 quad_perm:[1,0,3,2] row_mask:0xf bank_mask:0xf
	v_cndmask_b32_e64 v130, v126, v129, s[100:101]
	v_cndmask_b32_e64 v131, v128, v127, s[100:101]
	v_cvt_pk_bf16_f32 v130, v130, v131
	global_store_dword v[122:123], v130, off offset:3072
	v_mul_f32_e32 v126, v44, v112
	v_mul_f32_e32 v127, v45, v113
	s_nop 1
	v_mov_b32_dpp v128, v126 quad_perm:[1,0,3,2] row_mask:0xf bank_mask:0xf
	v_mov_b32_dpp v129, v127 quad_perm:[1,0,3,2] row_mask:0xf bank_mask:0xf
	v_cndmask_b32_e64 v130, v126, v129, s[100:101]
	v_cndmask_b32_e64 v131, v128, v127, s[100:101]
	v_cvt_pk_bf16_f32 v130, v130, v131
	global_store_dword v[122:123], v130, off offset:3136
	v_mul_f32_e32 v126, v28, v112
	v_mul_f32_e32 v127, v29, v113
	s_nop 1
	v_mov_b32_dpp v128, v126 quad_perm:[1,0,3,2] row_mask:0xf bank_mask:0xf
	v_mov_b32_dpp v129, v127 quad_perm:[1,0,3,2] row_mask:0xf bank_mask:0xf
	v_cndmask_b32_e64 v130, v126, v129, s[100:101]
	v_cndmask_b32_e64 v131, v128, v127, s[100:101]
	v_cvt_pk_bf16_f32 v130, v130, v131
	global_store_dword v[122:123], v130, off offset:3200
	v_mul_f32_e32 v126, v12, v112
	v_mul_f32_e32 v127, v13, v113
	s_nop 1
	v_mov_b32_dpp v128, v126 quad_perm:[1,0,3,2] row_mask:0xf bank_mask:0xf
	v_mov_b32_dpp v129, v127 quad_perm:[1,0,3,2] row_mask:0xf bank_mask:0xf
	v_cndmask_b32_e64 v130, v126, v129, s[100:101]
	v_cndmask_b32_e64 v131, v128, v127, s[100:101]
	v_cvt_pk_bf16_f32 v130, v130, v131
	global_store_dword v[122:123], v130, off offset:3264
	v_mov_b32_e32 v124, 0x1a000
	v_lshl_add_u64 v[122:123], v[120:121], 0, v[124:125]
	v_mul_f32_e32 v126, v62, v114
	v_mul_f32_e32 v127, v63, v115
	s_nop 1
	v_mov_b32_dpp v128, v126 quad_perm:[1,0,3,2] row_mask:0xf bank_mask:0xf
	v_mov_b32_dpp v129, v127 quad_perm:[1,0,3,2] row_mask:0xf bank_mask:0xf
	v_cndmask_b32_e64 v130, v126, v129, s[100:101]
	v_cndmask_b32_e64 v131, v128, v127, s[100:101]
	v_cvt_pk_bf16_f32 v130, v130, v131
	global_store_dword v[122:123], v130, off offset:3072
	v_mul_f32_e32 v126, v46, v114
	v_mul_f32_e32 v127, v47, v115
	s_nop 1
	v_mov_b32_dpp v128, v126 quad_perm:[1,0,3,2] row_mask:0xf bank_mask:0xf
	v_mov_b32_dpp v129, v127 quad_perm:[1,0,3,2] row_mask:0xf bank_mask:0xf
	v_cndmask_b32_e64 v130, v126, v129, s[100:101]
	v_cndmask_b32_e64 v131, v128, v127, s[100:101]
	v_cvt_pk_bf16_f32 v130, v130, v131
	global_store_dword v[122:123], v130, off offset:3136
	v_mul_f32_e32 v126, v30, v114
	v_mul_f32_e32 v127, v31, v115
	s_nop 1
	v_mov_b32_dpp v128, v126 quad_perm:[1,0,3,2] row_mask:0xf bank_mask:0xf
	v_mov_b32_dpp v129, v127 quad_perm:[1,0,3,2] row_mask:0xf bank_mask:0xf
	v_cndmask_b32_e64 v130, v126, v129, s[100:101]
	v_cndmask_b32_e64 v131, v128, v127, s[100:101]
	v_cvt_pk_bf16_f32 v130, v130, v131
	global_store_dword v[122:123], v130, off offset:3200
	v_mul_f32_e32 v126, v14, v114
	v_mul_f32_e32 v127, v15, v115
	s_nop 1
	v_mov_b32_dpp v128, v126 quad_perm:[1,0,3,2] row_mask:0xf bank_mask:0xf
	v_mov_b32_dpp v129, v127 quad_perm:[1,0,3,2] row_mask:0xf bank_mask:0xf
	v_cndmask_b32_e64 v130, v126, v129, s[100:101]
	v_cndmask_b32_e64 v131, v128, v127, s[100:101]
	v_cvt_pk_bf16_f32 v130, v130, v131
	global_store_dword v[122:123], v130, off offset:3264
	v_readlane_b32 s0, v254, 47
	s_add_i32 s18, s18, s0
	s_cmpk_gt_i32 s18, 0xff
	s_waitcnt vmcnt(63) expcnt(7) lgkmcnt(15)
	s_barrier
	s_cbranch_scc1 .LBB0_665
